# v21 + out-proj GEMM epilogue: the residual rows (64-B pieces shared by neighbouring waves of the workgroup) loaded through L1 (plain) instead of nt
# baseline (speedup 1.0000x reference)
;     __device__ __forceinline__ void operator()(const f32x4 (&acc)[2][2][4][2], const Unit& u, int wr, int wc, int fr, int fq) const {
;         const int row0 = u.pm * BM + wr * 64 + fr, col0 = u.pn * BM + wc * 32 + 8 * fq;
;         f32x4 gv[2][2];
; #pragma unroll
;         for (int bj = 0; bj < 2; ++bj)
; #pragma unroll
;             for (int n = 0; n < 2; ++n) gv[bj][n] = *(const f32x4*)(gate + col0 + bj * HALF + 4 * n) * *(const f32x4*)(cs + col0 + bj * HALF + 4 * n);
;         float rsv[2][4];
; #pragma unroll
;         for (int ai = 0; ai < 2; ++ai)
; #pragma unroll
;             for (int m = 0; m < 4; ++m) rsv[ai][m] = rs[row0 + ai * HALF + m * 16];
; #pragma unroll
;         for (int ai = 0; ai < 2; ++ai) {
;             u32x4 bwv[4][2];
; #pragma unroll
;             for (int m = 0; m < 4; ++m)
; #pragma unroll
;                 for (int bj = 0; bj < 2; ++bj) bwv[m][bj] = __builtin_nontemporal_load((const u32x4*)(base + (size_t)(row0 + ai * HALF + m * 16) * ldc + col0 + bj * HALF));
; #pragma unroll
;             for (int m = 0; m < 4; ++m) { const int row = row0 + ai * HALF + m * 16; const size_t off = (size_t)row * ldc + col0; const float rsc = rsv[ai][m];
; #pragma unroll
;                 for (int bj = 0; bj < 2; ++bj) {
;                     const u32x4 bw = bwv[m][bj];
;                     const f32x4 b0 = {__uint_as_float(bw.x << 16), __uint_as_float(bw.x & 0xffff0000u), __uint_as_float(bw.y << 16), __uint_as_float(bw.y & 0xffff0000u)};
;                     const f32x4 b1 = {__uint_as_float(bw.z << 16), __uint_as_float(bw.z & 0xffff0000u), __uint_as_float(bw.w << 16), __uint_as_float(bw.w & 0xffff0000u)};
;                     const i32x4 a0 = __builtin_bit_cast(i32x4, acc[ai][bj][m][0]), a1 = __builtin_bit_cast(i32x4, acc[ai][bj][m][1]);
;                     const f32x4 v0 = b0 + gv[bj][0] * ((f32x4){(float)a0[0], (float)a0[1], (float)a0[2], (float)a0[3]} * rsc), v1 = b1 + gv[bj][1] * ((f32x4){(float)a1[0], (float)a1[1], (float)a1[2], (float)a1[3]} * rsc);
;                     u32x4 w; w.x = cvt_pk_bf16(v0[0], v0[1]); w.y = cvt_pk_bf16(v0[2], v0[3]); w.z = cvt_pk_bf16(v1[0], v1[1]); w.w = cvt_pk_bf16(v1[2], v1[3]);
;                     *(u32x4*)(xb + off + bj * HALF) = w; }
.LBB0_977:
	v_lshl_or_b32 v130, s56, 8, v151
	v_ashrrev_i32_e32 v131, 31, v130
	v_lshl_add_u32 v136, s38, 8, v1
	v_ashrrev_i32_e32 v137, 31, v136
	v_lshlrev_b64 v[160:161], 1, v[130:131]
	v_lshlrev_b64 v[186:187], 12, v[136:137]
	v_lshl_add_u64 v[188:189], s[12:13], 0, v[160:161]
	v_lshlrev_b64 v[132:133], 2, v[130:131]
	v_lshl_add_u64 v[176:177], v[136:137], 2, s[8:9]
	v_lshl_add_u64 v[130:131], v[188:189], 0, v[186:187]
	v_lshl_add_u64 v[134:135], s[10:11], 0, v[132:133]
	v_lshl_add_u64 v[132:133], s[26:27], 0, v[132:133]
	global_load_dword v238, v[176:177], off
	global_load_dwordx4 v[164:167], v[134:135], off offset:16
	global_load_dwordx4 v[168:171], v[134:135], off
	global_load_dwordx4 v[172:175], v[132:133], off offset:16
	global_load_dwordx4 v[202:205], v[132:133], off
	global_load_dwordx4 v[206:209], v[134:135], off offset:528
	global_load_dwordx4 v[210:213], v[134:135], off offset:512
	global_load_dwordx4 v[214:217], v[132:133], off offset:528
	global_load_dwordx4 v[218:221], v[132:133], off offset:512
	global_load_dwordx4 v[222:225], v[130:131], off
	global_load_dwordx4 v[226:229], v[130:131], off offset:256
	v_cvt_f32_i32_e32 v244, v122
	v_or_b32_e32 v122, 16, v136
	v_cvt_f32_i32_e32 v245, v123
	v_ashrrev_i32_e32 v123, 31, v122
	v_lshlrev_b64 v[246:247], 12, v[122:123]
	v_cvt_f32_i32_e32 v179, v129
	v_cvt_f32_i32_e32 v178, v128
	v_lshl_add_u64 v[128:129], v[122:123], 2, s[8:9]
	v_lshl_add_u64 v[122:123], v[188:189], 0, v[246:247]
	global_load_dwordx4 v[230:233], v[122:123], off
	v_cvt_f32_i32_e32 v240, v126
	v_cvt_f32_i32_e32 v242, v124
	v_or_b32_e32 v124, 32, v136
	v_or_b32_e32 v126, 48, v136
	v_cvt_f32_i32_e32 v241, v127
	v_cvt_f32_i32_e32 v243, v125
	v_ashrrev_i32_e32 v125, 31, v124
	v_ashrrev_i32_e32 v127, 31, v126
	v_lshl_add_u64 v[130:131], v[124:125], 2, s[8:9]
	v_lshl_add_u64 v[132:133], v[126:127], 2, s[8:9]
	global_load_dword v184, v[176:177], off offset:512
	global_load_dword v182, v[176:177], off offset:576
	global_load_dword v180, v[176:177], off offset:640
	global_load_dword v248, v[128:129], off
	global_load_dword v196, v[130:131], off
	global_load_dword v192, v[132:133], off
	global_load_dword v162, v[176:177], off offset:704
	v_lshlrev_b64 v[198:199], 12, v[124:125]
	v_lshlrev_b64 v[194:195], 12, v[126:127]
	v_lshl_add_u64 v[124:125], v[188:189], 0, v[198:199]
	v_lshl_add_u64 v[176:177], v[188:189], 0, v[194:195]
	global_load_dwordx4 v[234:237], v[122:123], off offset:256
	global_load_dwordx4 v[134:137], v[124:125], off
	global_load_dwordx4 v[130:133], v[124:125], off offset:256
	global_load_dwordx4 v[126:129], v[176:177], off
	s_nop 0
	global_load_dwordx4 v[122:125], v[176:177], off offset:256
	v_cvt_f32_i32_e32 v121, v121
	v_cvt_f32_i32_e32 v119, v119
	v_cvt_f32_i32_e32 v118, v118
	v_cvt_f32_i32_e32 v120, v120
	v_cvt_f32_i32_e32 v117, v117
	v_cvt_f32_i32_e32 v115, v115
	v_cvt_f32_i32_e32 v114, v114
	v_cvt_f32_i32_e32 v116, v116
	v_cvt_f32_i32_e32 v111, v111
	v_cvt_f32_i32_e32 v110, v110
	v_cvt_f32_i32_e32 v109, v109
	v_cvt_f32_i32_e32 v107, v107
	v_cvt_f32_i32_e32 v106, v106
	v_cvt_f32_i32_e32 v108, v108
	v_cvt_f32_i32_e32 v113, v113
	v_cvt_f32_i32_e32 v112, v112
	v_cvt_f32_i32_e32 v105, v105
	v_cvt_f32_i32_e32 v103, v103
	v_cvt_f32_i32_e32 v102, v102
	v_cvt_f32_i32_e32 v104, v104
	v_cvt_f32_i32_e32 v101, v101
	v_cvt_f32_i32_e32 v99, v99
	v_cvt_f32_i32_e32 v98, v98
	v_cvt_f32_i32_e32 v100, v100
	v_cvt_f32_i32_e32 v95, v95
	v_cvt_f32_i32_e32 v94, v94
	v_cvt_f32_i32_e32 v93, v93
	v_cvt_f32_i32_e32 v91, v91
	v_cvt_f32_i32_e32 v90, v90
	v_cvt_f32_i32_e32 v92, v92
	v_cvt_f32_i32_e32 v97, v97
	v_cvt_f32_i32_e32 v96, v96
	v_cvt_f32_i32_e32 v89, v89
	v_cvt_f32_i32_e32 v87, v87
	v_cvt_f32_i32_e32 v86, v86
	v_cvt_f32_i32_e32 v88, v88
	v_cvt_f32_i32_e32 v85, v85
	v_cvt_f32_i32_e32 v83, v83
	v_cvt_f32_i32_e32 v82, v82
	v_cvt_f32_i32_e32 v84, v84
	v_cvt_f32_i32_e32 v79, v79
	v_cvt_f32_i32_e32 v78, v78
	v_cvt_f32_i32_e32 v77, v77
	v_cvt_f32_i32_e32 v75, v75
	s_waitcnt vmcnt(0)
	v_pk_mul_f32 v[240:241], v[238:239], v[240:241] op_sel_hi:[0,1]
	v_pk_mul_f32 v[250:251], v[238:239], v[178:179] op_sel_hi:[0,1]
	v_pk_mul_f32 v[244:245], v[238:239], v[244:245] op_sel_hi:[0,1]
	v_pk_mul_f32 v[172:173], v[164:165], v[172:173]
	v_pk_mul_f32 v[176:177], v[170:171], v[204:205]
	v_pk_mul_f32 v[178:179], v[168:169], v[202:203]
	v_pk_mul_f32 v[242:243], v[238:239], v[242:243] op_sel_hi:[0,1]
	v_pk_mul_f32 v[164:165], v[206:207], v[214:215]
	v_lshlrev_b32_e32 v202, 16, v222
	v_and_b32_e32 v203, 0xffff0000, v222
	v_lshlrev_b32_e32 v204, 16, v223
	v_and_b32_e32 v205, 0xffff0000, v223
	v_lshlrev_b32_e32 v206, 16, v224
	v_and_b32_e32 v207, 0xffff0000, v224
	v_pk_fma_f32 v[204:205], v[176:177], v[250:251], v[204:205]
	v_pk_fma_f32 v[202:203], v[178:179], v[240:241], v[202:203]
	v_pk_fma_f32 v[206:207], v[172:173], v[244:245], v[206:207]
	v_pk_mul_f32 v[174:175], v[166:167], v[174:175]
	v_pk_mul_f32 v[166:167], v[208:209], v[216:217]
	v_lshlrev_b32_e32 v208, 16, v225
	v_and_b32_e32 v209, 0xffff0000, v225
	v_cvt_pk_bf16_f32 v202, v202, v203
	v_cvt_pk_bf16_f32 v203, v204, v205
	v_cvt_pk_bf16_f32 v204, v206, v207
	v_lshl_add_u64 v[206:207], s[60:61], 0, v[186:187]
	v_pk_fma_f32 v[208:209], v[174:175], v[242:243], v[208:209]
	v_lshl_add_u64 v[206:207], v[206:207], 0, v[160:161]
	v_cvt_pk_bf16_f32 v205, v208, v209
	v_pk_mul_f32 v[168:169], v[212:213], v[220:221]
	v_pk_mul_f32 v[170:171], v[210:211], v[218:219]
	global_store_dwordx4 v[206:207], v[202:205], off
	v_lshlrev_b32_e32 v208, 16, v228
	v_and_b32_e32 v209, 0xffff0000, v228
	v_lshlrev_b32_e32 v202, 16, v226
	v_and_b32_e32 v203, 0xffff0000, v226
	v_lshlrev_b32_e32 v204, 16, v227
; __device__ __forceinline__ unsigned cvt_pk_bf16(float lo, float hi) { unsigned r; asm volatile("v_cvt_pk_bf16_f32 %0, %1, %2" : "=v"(r) : "v"(lo), "v"(hi)); return r; }
;     __device__ __forceinline__ void operator()(const f32x4 (&acc)[2][2][4][2], const Unit& u, int wr, int wc, int fr, int fq) const {
;     ...
;             for (int m = 0; m < 4; ++m) { const int row = row0 + ai * HALF + m * 16; const size_t off = (size_t)row * ldc + col0; const float rsc = rsv[ai][m];
; #pragma unroll
;                 for (int bj = 0; bj < 2; ++bj) {
;                     const u32x4 bw = bwv[m][bj];
;                     const f32x4 b0 = {__uint_as_float(bw.x << 16), __uint_as_float(bw.x & 0xffff0000u), __uint_as_float(bw.y << 16), __uint_as_float(bw.y & 0xffff0000u)};
;                     const f32x4 b1 = {__uint_as_float(bw.z << 16), __uint_as_float(bw.z & 0xffff0000u), __uint_as_float(bw.w << 16), __uint_as_float(bw.w & 0xffff0000u)};
;                     const i32x4 a0 = __builtin_bit_cast(i32x4, acc[ai][bj][m][0]), a1 = __builtin_bit_cast(i32x4, acc[ai][bj][m][1]);
;                     const f32x4 v0 = b0 + gv[bj][0] * ((f32x4){(float)a0[0], (float)a0[1], (float)a0[2], (float)a0[3]} * rsc), v1 = b1 + gv[bj][1] * ((f32x4){(float)a1[0], (float)a1[1], (float)a1[2], (float)a1[3]} * rsc);
;                     u32x4 w; w.x = cvt_pk_bf16(v0[0], v0[1]); w.y = cvt_pk_bf16(v0[2], v0[3]); w.z = cvt_pk_bf16(v1[0], v1[1]); w.w = cvt_pk_bf16(v1[2], v1[3]);
;                     *(u32x4*)(xb + off + bj * HALF) = w; }
	v_and_b32_e32 v205, 0xffff0000, v227
	v_lshlrev_b32_e32 v210, 16, v229
	v_and_b32_e32 v211, 0xffff0000, v229
	v_pk_mul_f32 v[118:119], v[238:239], v[118:119] op_sel_hi:[0,1]
	v_pk_mul_f32 v[120:121], v[238:239], v[120:121] op_sel_hi:[0,1]
	v_pk_mul_f32 v[114:115], v[238:239], v[114:115] op_sel_hi:[0,1]
	v_pk_mul_f32 v[116:117], v[238:239], v[116:117] op_sel_hi:[0,1]
	v_pk_fma_f32 v[120:121], v[168:169], v[120:121], v[204:205]
	v_pk_fma_f32 v[118:119], v[170:171], v[118:119], v[202:203]
	v_pk_fma_f32 v[202:203], v[166:167], v[116:117], v[210:211]
	v_pk_fma_f32 v[116:117], v[164:165], v[114:115], v[208:209]
	v_cvt_pk_bf16_f32 v114, v118, v119
	v_cvt_pk_bf16_f32 v115, v120, v121
	v_pk_mul_f32 v[110:111], v[248:249], v[110:111] op_sel_hi:[0,1]
	v_cvt_pk_bf16_f32 v116, v116, v117
	v_cvt_pk_bf16_f32 v117, v202, v203
	global_store_dwordx4 v[206:207], v[114:117], off offset:256
	v_lshlrev_b32_e32 v118, 16, v232
	v_and_b32_e32 v119, 0xffff0000, v232
	v_lshlrev_b32_e32 v114, 16, v230
	v_and_b32_e32 v115, 0xffff0000, v230
	v_lshlrev_b32_e32 v120, 16, v233
	v_and_b32_e32 v121, 0xffff0000, v233
	v_pk_fma_f32 v[110:111], v[178:179], v[110:111], v[114:115]
	v_pk_mul_f32 v[106:107], v[248:249], v[106:107] op_sel_hi:[0,1]
	v_pk_mul_f32 v[108:109], v[248:249], v[108:109] op_sel_hi:[0,1]
	v_lshlrev_b32_e32 v116, 16, v231
	v_and_b32_e32 v117, 0xffff0000, v231
	v_pk_mul_f32 v[112:113], v[248:249], v[112:113] op_sel_hi:[0,1]
	v_pk_fma_f32 v[114:115], v[174:175], v[108:109], v[120:121]
	v_pk_fma_f32 v[108:109], v[172:173], v[106:107], v[118:119]
	v_cvt_pk_bf16_f32 v106, v110, v111
	v_lshl_add_u64 v[110:111], s[60:61], 0, v[246:247]
	v_pk_fma_f32 v[112:113], v[176:177], v[112:113], v[116:117]
	v_lshl_add_u64 v[110:111], v[110:111], 0, v[160:161]
	v_cvt_pk_bf16_f32 v107, v112, v113
	v_cvt_pk_bf16_f32 v108, v108, v109
	v_cvt_pk_bf16_f32 v109, v114, v115
	global_store_dwordx4 v[110:111], v[106:109], off
	v_lshlrev_b32_e32 v112, 16, v236
	v_and_b32_e32 v113, 0xffff0000, v236
	v_lshlrev_b32_e32 v106, 16, v234
	v_and_b32_e32 v107, 0xffff0000, v234
	v_lshlrev_b32_e32 v108, 16, v235
	v_and_b32_e32 v109, 0xffff0000, v235
	v_lshlrev_b32_e32 v114, 16, v237
	v_and_b32_e32 v115, 0xffff0000, v237
	v_pk_mul_f32 v[102:103], v[248:249], v[102:103] op_sel_hi:[0,1]
	v_pk_mul_f32 v[104:105], v[248:249], v[104:105] op_sel_hi:[0,1]
	v_pk_mul_f32 v[98:99], v[248:249], v[98:99] op_sel_hi:[0,1]
	v_pk_mul_f32 v[100:101], v[248:249], v[100:101] op_sel_hi:[0,1]
	v_pk_fma_f32 v[104:105], v[168:169], v[104:105], v[108:109]
	v_pk_fma_f32 v[102:103], v[170:171], v[102:103], v[106:107]
	v_pk_fma_f32 v[106:107], v[166:167], v[100:101], v[114:115]
	v_pk_fma_f32 v[100:101], v[164:165], v[98:99], v[112:113]
	v_cvt_pk_bf16_f32 v98, v102, v103
	v_cvt_pk_bf16_f32 v99, v104, v105
	v_pk_mul_f32 v[94:95], v[196:197], v[94:95] op_sel_hi:[0,1]
	v_cvt_pk_bf16_f32 v100, v100, v101
	v_cvt_pk_bf16_f32 v101, v106, v107
	global_store_dwordx4 v[110:111], v[98:101], off offset:256
	v_lshlrev_b32_e32 v102, 16, v136
	v_and_b32_e32 v103, 0xffff0000, v136
	v_lshlrev_b32_e32 v98, 16, v134
	v_and_b32_e32 v99, 0xffff0000, v134
	v_lshlrev_b32_e32 v104, 16, v137
	v_and_b32_e32 v105, 0xffff0000, v137
	v_pk_fma_f32 v[94:95], v[178:179], v[94:95], v[98:99]
	v_pk_mul_f32 v[90:91], v[196:197], v[90:91] op_sel_hi:[0,1]
	v_pk_mul_f32 v[92:93], v[196:197], v[92:93] op_sel_hi:[0,1]
	v_lshlrev_b32_e32 v100, 16, v135
	v_and_b32_e32 v101, 0xffff0000, v135
	v_pk_mul_f32 v[96:97], v[196:197], v[96:97] op_sel_hi:[0,1]
	v_pk_fma_f32 v[98:99], v[174:175], v[92:93], v[104:105]
	v_pk_fma_f32 v[92:93], v[172:173], v[90:91], v[102:103]
	v_cvt_pk_bf16_f32 v90, v94, v95
	v_lshl_add_u64 v[94:95], s[60:61], 0, v[198:199]
	v_pk_fma_f32 v[96:97], v[176:177], v[96:97], v[100:101]
	v_lshl_add_u64 v[94:95], v[94:95], 0, v[160:161]
	v_cvt_pk_bf16_f32 v91, v96, v97
	v_cvt_pk_bf16_f32 v92, v92, v93
	v_cvt_pk_bf16_f32 v93, v98, v99
	v_cvt_f32_i32_e32 v74, v74
	v_cvt_f32_i32_e32 v76, v76
	global_store_dwordx4 v[94:95], v[90:93], off
	v_lshlrev_b32_e32 v96, 16, v132
	v_and_b32_e32 v97, 0xffff0000, v132
	v_lshlrev_b32_e32 v90, 16, v130
	v_and_b32_e32 v91, 0xffff0000, v130
	v_lshlrev_b32_e32 v92, 16, v131
	v_and_b32_e32 v93, 0xffff0000, v131
	v_lshlrev_b32_e32 v98, 16, v133
	v_and_b32_e32 v99, 0xffff0000, v133
	v_pk_mul_f32 v[86:87], v[196:197], v[86:87] op_sel_hi:[0,1]
	v_pk_mul_f32 v[88:89], v[196:197], v[88:89] op_sel_hi:[0,1]
	v_pk_mul_f32 v[82:83], v[196:197], v[82:83] op_sel_hi:[0,1]
	v_pk_mul_f32 v[84:85], v[196:197], v[84:85] op_sel_hi:[0,1]
	v_cvt_f32_i32_e32 v81, v81
	v_cvt_f32_i32_e32 v80, v80
	v_pk_fma_f32 v[88:89], v[168:169], v[88:89], v[92:93]
	v_pk_fma_f32 v[86:87], v[170:171], v[86:87], v[90:91]
	v_pk_fma_f32 v[90:91], v[166:167], v[84:85], v[98:99]
	v_pk_fma_f32 v[84:85], v[164:165], v[82:83], v[96:97]
	v_cvt_pk_bf16_f32 v82, v86, v87
	v_cvt_pk_bf16_f32 v83, v88, v89
	v_pk_mul_f32 v[78:79], v[192:193], v[78:79] op_sel_hi:[0,1]
	v_cvt_pk_bf16_f32 v84, v84, v85
	v_cvt_pk_bf16_f32 v85, v90, v91
	global_store_dwordx4 v[94:95], v[82:85], off offset:256
	v_cvt_f32_i32_e32 v71, v71
	v_cvt_f32_i32_e32 v70, v70
	v_lshlrev_b32_e32 v82, 16, v126
	v_and_b32_e32 v83, 0xffff0000, v126
	v_lshlrev_b32_e32 v86, 16, v128
	v_and_b32_e32 v87, 0xffff0000, v128
	v_lshlrev_b32_e32 v88, 16, v129
	v_and_b32_e32 v89, 0xffff0000, v129
	v_pk_fma_f32 v[78:79], v[178:179], v[78:79], v[82:83]
	v_pk_mul_f32 v[74:75], v[192:193], v[74:75] op_sel_hi:[0,1]
	v_pk_mul_f32 v[76:77], v[192:193], v[76:77] op_sel_hi:[0,1]
	v_cvt_f32_i32_e32 v69, v69
	v_cvt_f32_i32_e32 v67, v67
	v_cvt_f32_i32_e32 v66, v66
	v_cvt_f32_i32_e32 v68, v68
	v_lshlrev_b32_e32 v84, 16, v127
; __device__ __forceinline__ unsigned cvt_pk_bf16(float lo, float hi) { unsigned r; asm volatile("v_cvt_pk_bf16_f32 %0, %1, %2" : "=v"(r) : "v"(lo), "v"(hi)); return r; }
;     __device__ __forceinline__ void operator()(const f32x4 (&acc)[2][2][4][2], const Unit& u, int wr, int wc, int fr, int fq) const {
;     ...
;                 for (int bj = 0; bj < 2; ++bj) bwv[m][bj] = __builtin_nontemporal_load((const u32x4*)(base + (size_t)(row0 + ai * HALF + m * 16) * ldc + col0 + bj * HALF));
; #pragma unroll
;             for (int m = 0; m < 4; ++m) { const int row = row0 + ai * HALF + m * 16; const size_t off = (size_t)row * ldc + col0; const float rsc = rsv[ai][m];
; #pragma unroll
;                 for (int bj = 0; bj < 2; ++bj) {
;                     const u32x4 bw = bwv[m][bj];
;                     const f32x4 b0 = {__uint_as_float(bw.x << 16), __uint_as_float(bw.x & 0xffff0000u), __uint_as_float(bw.y << 16), __uint_as_float(bw.y & 0xffff0000u)};
;                     const f32x4 b1 = {__uint_as_float(bw.z << 16), __uint_as_float(bw.z & 0xffff0000u), __uint_as_float(bw.w << 16), __uint_as_float(bw.w & 0xffff0000u)};
;                     const i32x4 a0 = __builtin_bit_cast(i32x4, acc[ai][bj][m][0]), a1 = __builtin_bit_cast(i32x4, acc[ai][bj][m][1]);
;                     const f32x4 v0 = b0 + gv[bj][0] * ((f32x4){(float)a0[0], (float)a0[1], (float)a0[2], (float)a0[3]} * rsc), v1 = b1 + gv[bj][1] * ((f32x4){(float)a1[0], (float)a1[1], (float)a1[2], (float)a1[3]} * rsc);
;                     u32x4 w; w.x = cvt_pk_bf16(v0[0], v0[1]); w.y = cvt_pk_bf16(v0[2], v0[3]); w.z = cvt_pk_bf16(v1[0], v1[1]); w.w = cvt_pk_bf16(v1[2], v1[3]);
;                     *(u32x4*)(xb + off + bj * HALF) = w; }
	v_and_b32_e32 v85, 0xffff0000, v127
	v_pk_mul_f32 v[80:81], v[192:193], v[80:81] op_sel_hi:[0,1]
	v_pk_fma_f32 v[82:83], v[174:175], v[76:77], v[88:89]
	v_pk_fma_f32 v[76:77], v[172:173], v[74:75], v[86:87]
	v_cvt_pk_bf16_f32 v74, v78, v79
	v_lshl_add_u64 v[78:79], s[60:61], 0, v[194:195]
	v_cvt_f32_i32_e32 v73, v73
	v_cvt_f32_i32_e32 v72, v72
	v_pk_fma_f32 v[80:81], v[176:177], v[80:81], v[84:85]
	v_lshl_add_u64 v[78:79], v[78:79], 0, v[160:161]
	v_cvt_pk_bf16_f32 v75, v80, v81
	s_mov_b64 s[40:41], 0x80000
	v_cvt_pk_bf16_f32 v76, v76, v77
	v_cvt_pk_bf16_f32 v77, v82, v83
	global_store_dwordx4 v[78:79], v[74:77], off
	v_pk_mul_f32 v[70:71], v[192:193], v[70:71] op_sel_hi:[0,1]
	v_lshl_add_u64 v[190:191], v[186:187], 0, s[40:41]
	v_lshlrev_b32_e32 v74, 16, v122
	v_and_b32_e32 v75, 0xffff0000, v122
	v_lshlrev_b32_e32 v80, 16, v124
	v_and_b32_e32 v81, 0xffff0000, v124
	v_lshlrev_b32_e32 v82, 16, v125
	v_and_b32_e32 v83, 0xffff0000, v125
	v_pk_fma_f32 v[70:71], v[170:171], v[70:71], v[74:75]
	v_pk_mul_f32 v[66:67], v[192:193], v[66:67] op_sel_hi:[0,1]
	v_pk_mul_f32 v[68:69], v[192:193], v[68:69] op_sel_hi:[0,1]
	v_lshlrev_b32_e32 v76, 16, v123
	v_and_b32_e32 v77, 0xffff0000, v123
	v_pk_mul_f32 v[72:73], v[192:193], v[72:73] op_sel_hi:[0,1]
	v_pk_fma_f32 v[74:75], v[166:167], v[68:69], v[82:83]
	v_pk_fma_f32 v[68:69], v[164:165], v[66:67], v[80:81]
	v_cvt_pk_bf16_f32 v66, v70, v71
	v_lshl_add_u64 v[70:71], v[188:189], 0, v[190:191]
	v_pk_fma_f32 v[72:73], v[168:169], v[72:73], v[76:77]
	s_mov_b64 s[40:41], 0x90000
	v_cvt_pk_bf16_f32 v67, v72, v73
	v_cvt_pk_bf16_f32 v68, v68, v69
	v_cvt_pk_bf16_f32 v69, v74, v75
	global_load_dwordx4 v[86:89], v[70:71], off
	global_load_dwordx4 v[90:93], v[70:71], off offset:256
	v_lshl_add_u64 v[102:103], v[186:187], 0, s[40:41]
	v_lshl_add_u64 v[70:71], v[188:189], 0, v[102:103]
	global_load_dwordx4 v[94:97], v[70:71], off
	global_load_dwordx4 v[98:101], v[70:71], off offset:256
	s_mov_b64 s[40:41], 0xa0000
	v_lshl_add_u64 v[84:85], v[186:187], 0, s[40:41]
	global_store_dwordx4 v[78:79], v[66:69], off offset:256
	s_mov_b64 s[40:41], 0xb0000
	v_lshl_add_u64 v[82:83], v[186:187], 0, s[40:41]
	v_lshl_add_u64 v[66:67], v[188:189], 0, v[84:85]
	global_load_dwordx4 v[78:81], v[66:67], off
	global_load_dwordx4 v[74:77], v[66:67], off offset:256
	v_lshl_add_u64 v[66:67], v[188:189], 0, v[82:83]
	global_load_dwordx4 v[70:73], v[66:67], off
	s_nop 0
	global_load_dwordx4 v[66:69], v[66:67], off offset:256
	v_cvt_f32_i32_e32 v63, v63
	v_cvt_f32_i32_e32 v62, v62
	v_cvt_f32_i32_e32 v65, v65
	v_cvt_f32_i32_e32 v64, v64
	v_cvt_f32_i32_e32 v61, v61
	v_cvt_f32_i32_e32 v59, v59
	v_cvt_f32_i32_e32 v58, v58
	v_cvt_f32_i32_e32 v60, v60
	v_pk_mul_f32 v[62:63], v[184:185], v[62:63] op_sel_hi:[0,1]
	v_cvt_f32_i32_e32 v57, v57
	v_cvt_f32_i32_e32 v55, v55
	v_cvt_f32_i32_e32 v54, v54
	v_cvt_f32_i32_e32 v56, v56
	v_cvt_f32_i32_e32 v53, v53
	v_cvt_f32_i32_e32 v51, v51
	v_cvt_f32_i32_e32 v50, v50
	v_cvt_f32_i32_e32 v52, v52
	v_pk_mul_f32 v[64:65], v[184:185], v[64:65] op_sel_hi:[0,1]
	v_pk_mul_f32 v[58:59], v[184:185], v[58:59] op_sel_hi:[0,1]
	v_pk_mul_f32 v[60:61], v[184:185], v[60:61] op_sel_hi:[0,1]
	v_cvt_f32_i32_e32 v47, v47
	v_cvt_f32_i32_e32 v46, v46
	v_cvt_f32_i32_e32 v45, v45
	v_cvt_f32_i32_e32 v43, v43
	v_cvt_f32_i32_e32 v42, v42
	v_cvt_f32_i32_e32 v44, v44
	v_pk_mul_f32 v[54:55], v[184:185], v[54:55] op_sel_hi:[0,1]
	v_pk_mul_f32 v[56:57], v[184:185], v[56:57] op_sel_hi:[0,1]
	v_pk_mul_f32 v[50:51], v[184:185], v[50:51] op_sel_hi:[0,1]
	v_pk_mul_f32 v[52:53], v[184:185], v[52:53] op_sel_hi:[0,1]
	v_cvt_f32_i32_e32 v49, v49
	v_cvt_f32_i32_e32 v48, v48
	v_pk_mul_f32 v[46:47], v[182:183], v[46:47] op_sel_hi:[0,1]
	v_cvt_f32_i32_e32 v41, v41
	v_cvt_f32_i32_e32 v39, v39
	v_cvt_f32_i32_e32 v38, v38
	v_cvt_f32_i32_e32 v40, v40
	v_cvt_f32_i32_e32 v37, v37
	v_cvt_f32_i32_e32 v35, v35
	v_cvt_f32_i32_e32 v34, v34
	v_cvt_f32_i32_e32 v36, v36
	v_pk_mul_f32 v[42:43], v[182:183], v[42:43] op_sel_hi:[0,1]
	v_pk_mul_f32 v[44:45], v[182:183], v[44:45] op_sel_hi:[0,1]
	v_pk_mul_f32 v[48:49], v[182:183], v[48:49] op_sel_hi:[0,1]
	v_cvt_f32_i32_e32 v31, v31
	v_cvt_f32_i32_e32 v30, v30
	v_cvt_f32_i32_e32 v29, v29
	v_cvt_f32_i32_e32 v27, v27
	v_cvt_f32_i32_e32 v26, v26
	v_cvt_f32_i32_e32 v28, v28
	v_pk_mul_f32 v[38:39], v[182:183], v[38:39] op_sel_hi:[0,1]
	v_pk_mul_f32 v[40:41], v[182:183], v[40:41] op_sel_hi:[0,1]
	v_pk_mul_f32 v[34:35], v[182:183], v[34:35] op_sel_hi:[0,1]
	v_pk_mul_f32 v[36:37], v[182:183], v[36:37] op_sel_hi:[0,1]
	v_cvt_f32_i32_e32 v33, v33
	v_cvt_f32_i32_e32 v32, v32
	v_pk_mul_f32 v[30:31], v[180:181], v[30:31] op_sel_hi:[0,1]
	v_cvt_f32_i32_e32 v25, v25
	v_cvt_f32_i32_e32 v23, v23
	v_cvt_f32_i32_e32 v22, v22
	v_cvt_f32_i32_e32 v24, v24
	v_cvt_f32_i32_e32 v21, v21
	v_cvt_f32_i32_e32 v19, v19
	v_cvt_f32_i32_e32 v18, v18
	v_cvt_f32_i32_e32 v20, v20
	s_waitcnt vmcnt(8)
	v_lshlrev_b32_e32 v104, 16, v86
	v_and_b32_e32 v105, 0xffff0000, v86
	v_lshlrev_b32_e32 v86, 16, v87
	v_and_b32_e32 v87, 0xffff0000, v87
	v_lshlrev_b32_e32 v106, 16, v88
	v_and_b32_e32 v107, 0xffff0000, v88
	v_lshlrev_b32_e32 v88, 16, v89
	v_and_b32_e32 v89, 0xffff0000, v89
	v_pk_fma_f32 v[62:63], v[178:179], v[62:63], v[104:105]
	v_pk_fma_f32 v[64:65], v[176:177], v[64:65], v[86:87]
	v_pk_fma_f32 v[86:87], v[174:175], v[60:61], v[88:89]
	v_pk_fma_f32 v[60:61], v[172:173], v[58:59], v[106:107]
	v_cvt_pk_bf16_f32 v58, v62, v63
	v_lshl_add_u64 v[62:63], s[60:61], 0, v[190:191]
	v_cvt_pk_bf16_f32 v59, v64, v65
	v_cvt_pk_bf16_f32 v60, v60, v61
	v_cvt_pk_bf16_f32 v61, v86, v87
	v_lshl_add_u64 v[62:63], v[62:63], 0, v[160:161]
	global_store_dwordx4 v[62:63], v[58:61], off
	s_waitcnt vmcnt(8)
; __device__ __forceinline__ unsigned cvt_pk_bf16(float lo, float hi) { unsigned r; asm volatile("v_cvt_pk_bf16_f32 %0, %1, %2" : "=v"(r) : "v"(lo), "v"(hi)); return r; }
; #define PG8_BAR __builtin_amdgcn_s_barrier()
; template <class Epi, class Sched, bool ALIGN_EPI = false, bool SP2 = false, bool I8 = false>
; __device__ __forceinline__ void gemm_phase(PG8_LAS unsigned char* lds, const Gemm g, const Sched& S, const Epi& E) {
;     ...
;         if constexpr (ALIGN_EPI) { if (wr == 0) PG8_BAR; }
;         if constexpr (!Epi::AFTER_DRAIN) { E(acc, cur, wr, wc, fr, fq); S.done(cur); }
;         if (!has_next) break;
; #pragma unroll
;         for (int a = 0; a < 2; ++a)
; #pragma unroll
;             for (int b = 0; b < 2; ++b)
; #pragma unroll
;                 for (int m = 0; m < 4; ++m)
; #pragma unroll
;                     for (int n = 0; n < 2; ++n) acc[a][b][m][n] = (f32x4){0.f, 0.f, 0.f, 0.f};
;         cur = nxt; cA = nA; cB = nB; ++ui;
;         if constexpr (ALIGN_EPI) { if (wr == 1) PG8_BAR; }
;     __device__ __forceinline__ void operator()(const f32x4 (&acc)[2][2][4][2], const Unit& u, int wr, int wc, int fr, int fq) const {
;     ...
;             for (int m = 0; m < 4; ++m) { const int row = row0 + ai * HALF + m * 16; const size_t off = (size_t)row * ldc + col0; const float rsc = rsv[ai][m];
; #pragma unroll
;                 for (int bj = 0; bj < 2; ++bj) {
;                     const u32x4 bw = bwv[m][bj];
;                     const f32x4 b0 = {__uint_as_float(bw.x << 16), __uint_as_float(bw.x & 0xffff0000u), __uint_as_float(bw.y << 16), __uint_as_float(bw.y & 0xffff0000u)};
;                     const f32x4 b1 = {__uint_as_float(bw.z << 16), __uint_as_float(bw.z & 0xffff0000u), __uint_as_float(bw.w << 16), __uint_as_float(bw.w & 0xffff0000u)};
;                     const i32x4 a0 = __builtin_bit_cast(i32x4, acc[ai][bj][m][0]), a1 = __builtin_bit_cast(i32x4, acc[ai][bj][m][1]);
;                     const f32x4 v0 = b0 + gv[bj][0] * ((f32x4){(float)a0[0], (float)a0[1], (float)a0[2], (float)a0[3]} * rsc), v1 = b1 + gv[bj][1] * ((f32x4){(float)a1[0], (float)a1[1], (float)a1[2], (float)a1[3]} * rsc);
;                     u32x4 w; w.x = cvt_pk_bf16(v0[0], v0[1]); w.y = cvt_pk_bf16(v0[2], v0[3]); w.z = cvt_pk_bf16(v1[0], v1[1]); w.w = cvt_pk_bf16(v1[2], v1[3]);
;                     *(u32x4*)(xb + off + bj * HALF) = w; }
	v_lshlrev_b32_e32 v64, 16, v92
	v_and_b32_e32 v65, 0xffff0000, v92
	v_lshlrev_b32_e32 v58, 16, v90
	v_and_b32_e32 v59, 0xffff0000, v90
	v_lshlrev_b32_e32 v60, 16, v91
	v_and_b32_e32 v61, 0xffff0000, v91
	v_lshlrev_b32_e32 v86, 16, v93
	v_and_b32_e32 v87, 0xffff0000, v93
	v_pk_fma_f32 v[56:57], v[168:169], v[56:57], v[60:61]
	v_pk_fma_f32 v[54:55], v[170:171], v[54:55], v[58:59]
	v_pk_fma_f32 v[58:59], v[166:167], v[52:53], v[86:87]
	v_pk_fma_f32 v[52:53], v[164:165], v[50:51], v[64:65]
	v_cvt_pk_bf16_f32 v50, v54, v55
	v_cvt_pk_bf16_f32 v51, v56, v57
	s_waitcnt vmcnt(7)
	v_lshlrev_b32_e32 v54, 16, v96
	v_cvt_pk_bf16_f32 v52, v52, v53
	v_cvt_pk_bf16_f32 v53, v58, v59
	global_store_dwordx4 v[62:63], v[50:53], off offset:256
	v_and_b32_e32 v55, 0xffff0000, v96
	v_lshlrev_b32_e32 v56, 16, v97
	v_lshlrev_b32_e32 v50, 16, v94
	v_and_b32_e32 v51, 0xffff0000, v94
	v_and_b32_e32 v57, 0xffff0000, v97
	v_pk_fma_f32 v[46:47], v[178:179], v[46:47], v[50:51]
	v_lshlrev_b32_e32 v52, 16, v95
	v_and_b32_e32 v53, 0xffff0000, v95
	v_pk_fma_f32 v[50:51], v[174:175], v[44:45], v[56:57]
	v_pk_fma_f32 v[44:45], v[172:173], v[42:43], v[54:55]
	v_cvt_pk_bf16_f32 v42, v46, v47
	v_lshl_add_u64 v[46:47], s[60:61], 0, v[102:103]
	v_pk_fma_f32 v[48:49], v[176:177], v[48:49], v[52:53]
	v_lshl_add_u64 v[46:47], v[46:47], 0, v[160:161]
	v_cvt_pk_bf16_f32 v43, v48, v49
	v_cvt_pk_bf16_f32 v44, v44, v45
	v_cvt_pk_bf16_f32 v45, v50, v51
	global_store_dwordx4 v[46:47], v[42:45], off
	s_waitcnt vmcnt(8)
	v_lshlrev_b32_e32 v48, 16, v100
	v_and_b32_e32 v49, 0xffff0000, v100
	v_lshlrev_b32_e32 v42, 16, v98
	v_and_b32_e32 v43, 0xffff0000, v98
	v_lshlrev_b32_e32 v44, 16, v99
	v_and_b32_e32 v45, 0xffff0000, v99
	v_lshlrev_b32_e32 v50, 16, v101
	v_and_b32_e32 v51, 0xffff0000, v101
	v_pk_fma_f32 v[40:41], v[168:169], v[40:41], v[44:45]
	v_pk_fma_f32 v[38:39], v[170:171], v[38:39], v[42:43]
	v_pk_fma_f32 v[42:43], v[166:167], v[36:37], v[50:51]
	v_pk_fma_f32 v[36:37], v[164:165], v[34:35], v[48:49]
	v_cvt_pk_bf16_f32 v34, v38, v39
	v_cvt_pk_bf16_f32 v35, v40, v41
	s_waitcnt vmcnt(6)
	v_lshlrev_b32_e32 v38, 16, v80
	v_cvt_pk_bf16_f32 v36, v36, v37
	v_cvt_pk_bf16_f32 v37, v42, v43
	global_store_dwordx4 v[46:47], v[34:37], off offset:256
	v_and_b32_e32 v39, 0xffff0000, v80
	v_lshlrev_b32_e32 v40, 16, v81
	v_lshlrev_b32_e32 v34, 16, v78
	v_and_b32_e32 v35, 0xffff0000, v78
	v_and_b32_e32 v41, 0xffff0000, v81
	v_pk_fma_f32 v[30:31], v[178:179], v[30:31], v[34:35]
	v_pk_mul_f32 v[26:27], v[180:181], v[26:27] op_sel_hi:[0,1]
	v_pk_mul_f32 v[28:29], v[180:181], v[28:29] op_sel_hi:[0,1]
	v_lshlrev_b32_e32 v36, 16, v79
	v_and_b32_e32 v37, 0xffff0000, v79
	v_pk_mul_f32 v[32:33], v[180:181], v[32:33] op_sel_hi:[0,1]
	v_pk_fma_f32 v[34:35], v[174:175], v[28:29], v[40:41]
	v_pk_fma_f32 v[28:29], v[172:173], v[26:27], v[38:39]
	v_cvt_pk_bf16_f32 v26, v30, v31
	v_lshl_add_u64 v[30:31], s[60:61], 0, v[84:85]
	v_cvt_f32_i32_e32 v15, v15
	v_cvt_f32_i32_e32 v14, v14
	v_pk_fma_f32 v[32:33], v[176:177], v[32:33], v[36:37]
	v_lshl_add_u64 v[30:31], v[30:31], 0, v[160:161]
	v_cvt_pk_bf16_f32 v27, v32, v33
	v_cvt_pk_bf16_f32 v28, v28, v29
	v_cvt_pk_bf16_f32 v29, v34, v35
	v_cvt_f32_i32_e32 v13, v13
	v_cvt_f32_i32_e32 v11, v11
	v_cvt_f32_i32_e32 v10, v10
	v_cvt_f32_i32_e32 v12, v12
	global_store_dwordx4 v[30:31], v[26:29], off
	s_waitcnt vmcnt(7)
	v_lshlrev_b32_e32 v32, 16, v76
	v_and_b32_e32 v33, 0xffff0000, v76
	v_lshlrev_b32_e32 v26, 16, v74
	v_and_b32_e32 v27, 0xffff0000, v74
	v_lshlrev_b32_e32 v28, 16, v75
	v_and_b32_e32 v29, 0xffff0000, v75
	v_lshlrev_b32_e32 v34, 16, v77
	v_and_b32_e32 v35, 0xffff0000, v77
	v_pk_mul_f32 v[22:23], v[180:181], v[22:23] op_sel_hi:[0,1]
	v_pk_mul_f32 v[24:25], v[180:181], v[24:25] op_sel_hi:[0,1]
	v_pk_mul_f32 v[18:19], v[180:181], v[18:19] op_sel_hi:[0,1]
	v_pk_mul_f32 v[20:21], v[180:181], v[20:21] op_sel_hi:[0,1]
	v_cvt_f32_i32_e32 v17, v17
	v_cvt_f32_i32_e32 v16, v16
	v_pk_fma_f32 v[24:25], v[168:169], v[24:25], v[28:29]
	v_pk_fma_f32 v[22:23], v[170:171], v[22:23], v[26:27]
	v_pk_fma_f32 v[26:27], v[166:167], v[20:21], v[34:35]
	v_pk_fma_f32 v[20:21], v[164:165], v[18:19], v[32:33]
	v_cvt_pk_bf16_f32 v18, v22, v23
	v_cvt_pk_bf16_f32 v19, v24, v25
	v_pk_mul_f32 v[14:15], v[162:163], v[14:15] op_sel_hi:[0,1]
	v_cvt_pk_bf16_f32 v20, v20, v21
	v_cvt_pk_bf16_f32 v21, v26, v27
	global_store_dwordx4 v[30:31], v[18:21], off offset:256
	v_cvt_f32_i32_e32 v7, v7
	v_cvt_f32_i32_e32 v6, v6
	s_waitcnt vmcnt(7)
	v_lshlrev_b32_e32 v18, 16, v70
	v_and_b32_e32 v19, 0xffff0000, v70
	v_cvt_f32_i32_e32 v5, v5
	v_cvt_f32_i32_e32 v3, v3
	v_cvt_f32_i32_e32 v2, v2
	v_cvt_f32_i32_e32 v4, v4
	v_lshlrev_b32_e32 v22, 16, v72
	v_and_b32_e32 v23, 0xffff0000, v72
	v_lshlrev_b32_e32 v24, 16, v73
	v_and_b32_e32 v25, 0xffff0000, v73
	v_pk_fma_f32 v[14:15], v[178:179], v[14:15], v[18:19]
	v_pk_mul_f32 v[10:11], v[162:163], v[10:11] op_sel_hi:[0,1]
	v_pk_mul_f32 v[12:13], v[162:163], v[12:13] op_sel_hi:[0,1]
	v_cvt_f32_i32_e32 v9, v9
	v_cvt_f32_i32_e32 v8, v8
	v_lshlrev_b32_e32 v20, 16, v71
	v_and_b32_e32 v21, 0xffff0000, v71
	v_pk_mul_f32 v[16:17], v[162:163], v[16:17] op_sel_hi:[0,1]
	v_pk_fma_f32 v[18:19], v[174:175], v[12:13], v[24:25]
	v_pk_fma_f32 v[12:13], v[172:173], v[10:11], v[22:23]
	v_cvt_pk_bf16_f32 v10, v14, v15
	v_lshl_add_u64 v[14:15], s[60:61], 0, v[82:83]
	v_pk_fma_f32 v[16:17], v[176:177], v[16:17], v[20:21]
	v_lshl_add_u64 v[14:15], v[14:15], 0, v[160:161]
	v_cvt_pk_bf16_f32 v11, v16, v17
	v_cvt_pk_bf16_f32 v12, v12, v13
	v_cvt_pk_bf16_f32 v13, v18, v19
	global_store_dwordx4 v[14:15], v[10:13], off
	s_waitcnt vmcnt(7)
	v_lshlrev_b32_e32 v16, 16, v68
	v_and_b32_e32 v17, 0xffff0000, v68
	v_lshlrev_b32_e32 v10, 16, v66
	v_and_b32_e32 v11, 0xffff0000, v66
	v_lshlrev_b32_e32 v18, 16, v69
	v_and_b32_e32 v19, 0xffff0000, v69
	v_pk_mul_f32 v[6:7], v[162:163], v[6:7] op_sel_hi:[0,1]
	v_pk_mul_f32 v[2:3], v[162:163], v[2:3] op_sel_hi:[0,1]
	v_pk_mul_f32 v[4:5], v[162:163], v[4:5] op_sel_hi:[0,1]
	v_lshlrev_b32_e32 v12, 16, v67
	v_and_b32_e32 v13, 0xffff0000, v67
	v_pk_mul_f32 v[8:9], v[162:163], v[8:9] op_sel_hi:[0,1]
	v_pk_fma_f32 v[6:7], v[170:171], v[6:7], v[10:11]
	v_pk_fma_f32 v[10:11], v[166:167], v[4:5], v[18:19]
	v_pk_fma_f32 v[4:5], v[164:165], v[2:3], v[16:17]
	s_andn2_b64 vcc, exec, s[0:1]
	s_mov_b64 s[0:1], -1
	s_mov_b32 s58, s84
	v_pk_fma_f32 v[8:9], v[168:169], v[8:9], v[12:13]
	v_cvt_pk_bf16_f32 v2, v6, v7
	s_nop 0
	v_cvt_pk_bf16_f32 v3, v8, v9
	v_cvt_pk_bf16_f32 v4, v4, v5
	v_cvt_pk_bf16_f32 v5, v10, v11
	global_store_dwordx4 v[14:15], v[2:5], off offset:256
	s_cbranch_vccnz .LBB0_966
	s_andn2_b64 vcc, exec, s[2:3]
	s_cbranch_vccnz .LBB0_965
	s_barrier
	s_branch .LBB0_965
